# v036 + topk unmono() as v_ashrrev + v_bitop3 (~(t ^ (key & (mask & 0x7fffffff)))) at 27 sites
# baseline (speedup 1.0000x reference)
; #define LAS __attribute__((address_space(3)))
; __device__ __forceinline__ int phase_tid() { int t = (int)threadIdx.x; asm volatile("" : "+v"(t)); return t; }
; __device__ __forceinline__ int phase_wid(int tid) { return __builtin_amdgcn_readfirstlane(tid >> 6); }
; __device__ __forceinline__ void topk_phase(LAS unsigned char* lds, const bf16_t* qp, const bf16_t* keys, const float* SU, const float* SV, int* sel_e, float* sel_g, float* sel_su, int G, int b) {
;     const int tid = phase_tid(), lane = tid & 63, wid = phase_wid(tid), fr = lane & 15, fq = lane >> 4;
;     LAS unsigned* wl = (LAS unsigned*)(lds + wid * 4096 + fr * 256);
;     LAS bf16_t* KL = (LAS bf16_t*)(lds + 32768);
;     pg8::StaticOrder SO; SO.init(S_, D_, G, b);
;     u32x4 kpre[8];
;     const int krow = tid >> 1, khf = tid & 1;
;     for (int ui = 0; ; ++ui) {
;         pg8::Unit gu; if (!SO.next(ui >> 1, gu)) break;
;         const int tt = gu.pm * 2 + (ui & 1), h = gu.pn;
;         const int tok = tt * 128 + wid * 16 + fr;
;         if ((ui & 1) == 0) {
.LBB0_633:
	s_add_u32 s46, s92, 0x13800000
	s_addc_u32 s47, s93, 0
	s_add_u32 s48, s92, 0x14000000
	s_addc_u32 s49, s93, 0
	v_mov_b32_e32 v6, v0
	s_waitcnt vmcnt(0)
	s_barrier
	s_add_u32 s54, s92, 0x1c800000
	s_addc_u32 s55, s93, 0
	v_readfirstlane_b32 s0, v6
	v_ashrrev_i32_e32 v2, 1, v6
	s_ashr_i32 s0, s0, 6
	v_ashrrev_i32_e32 v3, 31, v2
	s_lshl_b32 s1, s0, 12
	v_lshlrev_b64 v[4:5], 8, v[2:3]
	v_lshlrev_b32_e32 v3, 7, v6
	v_and_b32_e32 v7, 15, v6
	s_add_i32 s1, s1, 0
	v_lshl_add_u64 v[4:5], s[92:93], 0, v[4:5]
	v_and_b32_e32 v78, 0x80, v3
	v_mov_b32_e32 v79, 0
	v_lshl_add_u32 v83, v7, 8, s1
	v_lshl_or_b32 v85, s0, 4, v7
	v_lshl_add_u64 v[4:5], v[4:5], 0, v[78:79]
	s_mov_b64 s[0:1], 0x1100000
	v_bfe_u32 v1, v6, 4, 2
	v_lshl_add_u64 v[80:81], v[4:5], 0, s[0:1]
	s_movk_i32 s0, 0x110
	v_mul_lo_u32 v2, v2, s0
	v_lshl_add_u32 v87, v1, 4, 0
	v_add_u32_e32 v3, 0, v2
	v_lshlrev_b32_e32 v2, 3, v1
	v_add_u32_e32 v4, 0x8000, v87
	v_lshlrev_b32_e32 v82, 2, v1
	v_mul_u32_u24_e32 v89, 0x110, v7
	s_mov_b32 s52, 0
	v_cmp_eq_u32_e64 s[38:39], 2, v1
	v_cmp_eq_u32_e64 s[40:41], 0, v1
	v_cmp_ne_u32_e64 s[42:43], 0, v1
	v_xor_b32_e32 v98, 0x7f, v82
	v_xor_b32_e32 v99, 63, v82
	v_xor_b32_e32 v100, 0x7e, v82
	v_xor_b32_e32 v101, 62, v82
	v_xor_b32_e32 v102, 0x7d, v82
	v_xor_b32_e32 v103, 61, v82
	v_xor_b32_e32 v104, 0x7c, v82
	v_xor_b32_e32 v105, 60, v82
	v_xor_b32_e32 v106, 0x6f, v82
	v_xor_b32_e32 v107, 47, v82
	v_xor_b32_e32 v108, 0x6e, v82
	v_xor_b32_e32 v109, 46, v82
	v_xor_b32_e32 v110, 0x6d, v82
	v_xor_b32_e32 v111, 45, v82
	v_xor_b32_e32 v112, 0x6c, v82
	v_xor_b32_e32 v113, 44, v82
	v_xor_b32_e32 v114, 0x5f, v82
	v_xor_b32_e32 v115, 31, v82
	v_xor_b32_e32 v116, 0x5e, v82
	v_xor_b32_e32 v117, 30, v82
	v_xor_b32_e32 v118, 0x5d, v82
	v_xor_b32_e32 v119, 29, v82
	v_xor_b32_e32 v120, 0x5c, v82
	v_xor_b32_e32 v121, 28, v82
	v_xor_b32_e32 v122, 0x4f, v82
	v_xor_b32_e32 v123, 15, v82
	v_xor_b32_e32 v124, 0x4e, v82
	v_xor_b32_e32 v125, 14, v82
	v_xor_b32_e32 v126, 0x4d, v82
	v_xor_b32_e32 v127, 13, v82
	v_xor_b32_e32 v128, 0x4c, v82
	v_xor_b32_e32 v129, 12, v82
	v_or_b32_e32 v84, 1, v82
	v_or_b32_e32 v86, 2, v82
	v_or_b32_e32 v88, 3, v82
	v_add_u32_e32 v130, v3, v78
	v_lshlrev_b32_e32 v78, 1, v2
	s_movk_i32 s53, 0xff80
	s_mov_b32 s12, 0x7fffff80
	s_mov_b32 s13, 0x7fffff00
	s_mov_b32 s14, 0x7fffffff
	v_add_u32_e32 v131, v4, v89
	s_movk_i32 s60, 0xff00
	s_movk_i32 s61, 0x3fff
	v_mov_b64_e32 v[90:91], 0x200
	v_mov_b64_e32 v[92:93], 0x1ff
	v_bfrev_b32_e32 v132, 1
	v_mov_b32_e32 v133, 0xffffff00
	s_branch .LBB0_637

; __device__ __forceinline__ unsigned mono(float f) { const unsigned u = __float_as_uint(f); return (u & 0x80000000u) ? ~u : (u ^ 0x80000000u); }
; __device__ __forceinline__ float unmono(unsigned u) { return __uint_as_float((u & 0x80000000u) ? (u ^ 0x80000000u) : ~u); }
; __device__ __forceinline__ void topk_phase(LAS unsigned char* lds, const bf16_t* qp, const bf16_t* keys, const float* SU, const float* SV, int* sel_e, float* sel_g, float* sel_su, int G, int b) {
;     ...
;         float v1[16], v2[16];
; #pragma unroll
;         for (int i = 0; i < 16; ++i) { v1[i] = unmono(T[0][i] & ~127u); v2[i] = unmono(T[1][i] & ~127u); }
;         unsigned ck[16];
; #pragma unroll
;         for (int sidx = 0; sidx < 13; ++sidx) {
;             unsigned keyk[4];
; #pragma unroll
;             for (int k = 0; k < 4; ++k) {
;                 const int c = 4 * sidx + k;
;                 if (c < 50) { const int ci = cand_i(c), cj = cand_j(c); keyk[k] = (mono(v1[ci] + v2[cj]) & ~255u) | (unsigned)(255 - (ci * 16 + cj)); }
;                 else keyk[k] = 0u;
;             }
;             ck[sidx] = fq == 0 ? keyk[0] : fq == 1 ? keyk[1] : fq == 2 ? keyk[2] : keyk[3];
.LBB0_665:
	s_or_b64 exec, exec, s[0:1]
	v_min_u32_e32 v36, v36, v44
	v_min_u32_e32 v37, v37, v45
	v_min_u32_e32 v42, v42, v69
	v_min_u32_e32 v44, v43, v147
	v_max_u32_e32 v45, v36, v42
	v_max_u32_e32 v69, v37, v44
	v_min_u32_e32 v36, v36, v42
	v_min_u32_e32 v37, v37, v44
	v_min_u32_e32 v43, v45, v69
	v_max_u32_e32 v42, v45, v69
	v_min_u32_e32 v45, v36, v37
	v_max_u32_e32 v44, v36, v37
	v_cmp_lt_i32_e64 s[0:1], -1, v45
	v_ashrrev_i32_e32 v147, 31, v43
	v_bitop3_b32 v148, v43, v147, s12 bitop3:0x93
	v_cndmask_b32_e64 v37, v132, -1, s[0:1]
	v_cmp_lt_i32_e64 s[0:1], -1, v44
	v_and_b32_e32 v36, 0xffffff80, v45
	v_and_b32_e32 v69, 0xffffff80, v44
	v_cndmask_b32_e64 v147, v132, -1, s[0:1]
	v_cmp_lt_i32_e32 vcc, -1, v42
	v_xor_b32_e32 v37, v37, v36
	v_xor_b32_e32 v36, v147, v69
	v_cmp_lt_i32_e64 s[0:1], 0, v1
	s_and_saveexec_b64 s[4:5], s[0:1]
	s_xor_b64 s[4:5], exec, s[4:5]
	s_cbranch_execz .LBB0_669
	v_add_f32_e32 v69, v54, v148
	v_cmp_lt_i32_e64 s[0:1], -1, v69
	s_nop 1
	v_cndmask_b32_e64 v147, -1, v132, s[0:1]
	v_bitop3_b32 v69, v147, s60, v69 bitop3:0x48
	v_or_b32_e32 v69, 0xfa, v69
	v_cmp_ne_u32_e64 s[0:1], 1, v1
	s_and_saveexec_b64 s[6:7], s[0:1]
	s_cbranch_execz .LBB0_668
	v_pk_add_f32 v[154:155], v[54:55], v[36:37] op_sel_hi:[0,1]
	v_cmp_lt_i32_e64 s[0:1], -1, v155
	v_and_b32_e32 v147, 0xffffff00, v155
	s_nop 0
	v_cndmask_b32_e64 v69, v133, v132, s[0:1]
	s_movk_i32 s0, 0xf8
	v_bitop3_b32 v69, v69, s0, v147 bitop3:0xde
	v_cmp_lt_i32_e64 s[0:1], -1, v154
	v_and_b32_e32 v154, 0xffffff00, v154
	s_nop 0
	v_cndmask_b32_e64 v147, v133, v132, s[0:1]
	s_movk_i32 s0, 0xf9
	v_bitop3_b32 v147, v147, s0, v154 bitop3:0xde
	v_cndmask_b32_e64 v69, v69, v147, s[38:39]

; __device__ __forceinline__ unsigned mono(float f) { const unsigned u = __float_as_uint(f); return (u & 0x80000000u) ? ~u : (u ^ 0x80000000u); }
; __device__ __forceinline__ float unmono(unsigned u) { return __uint_as_float((u & 0x80000000u) ? (u ^ 0x80000000u) : ~u); }
; __device__ __forceinline__ void topk_phase(LAS unsigned char* lds, const bf16_t* qp, const bf16_t* keys, const float* SU, const float* SV, int* sel_e, float* sel_g, float* sel_su, int G, int b) {
;     ...
;         float v1[16], v2[16];
; #pragma unroll
;         for (int i = 0; i < 16; ++i) { v1[i] = unmono(T[0][i] & ~127u); v2[i] = unmono(T[1][i] & ~127u); }
;         unsigned ck[16];
; #pragma unroll
;         for (int sidx = 0; sidx < 13; ++sidx) {
;             unsigned keyk[4];
; #pragma unroll
;             for (int k = 0; k < 4; ++k) {
;                 const int c = 4 * sidx + k;
;                 if (c < 50) { const int ci = cand_i(c), cj = cand_j(c); keyk[k] = (mono(v1[ci] + v2[cj]) & ~255u) | (unsigned)(255 - (ci * 16 + cj)); }
;                 else keyk[k] = 0u;
;             }
;             ck[sidx] = fq == 0 ? keyk[0] : fq == 1 ? keyk[1] : fq == 2 ? keyk[2] : keyk[3];
.LBB0_669:
	s_or_saveexec_b64 s[0:1], s[4:5]
	v_cndmask_b32_e64 v147, v132, -1, vcc
	v_bitop3_b32 v147, v147, v42, s53 bitop3:0x78
	s_xor_b64 exec, exec, s[0:1]
	v_add_f32_e32 v69, v54, v147
	v_cmp_lt_i32_e32 vcc, -1, v69
	s_nop 1
	v_cndmask_b32_e32 v154, -1, v132, vcc
	v_bitop3_b32 v69, v154, s60, v69 bitop3:0x48
	v_or_b32_e32 v69, 0xfb, v69
	s_or_b64 exec, exec, s[0:1]
	v_min_u32_e32 v154, v46, v97
	v_min_u32_e32 v134, v47, v134
	v_min_u32_e32 v143, v48, v143
	v_min_u32_e32 v149, v49, v149
	v_min_u32_e32 v50, v50, v150
	v_min_u32_e32 v51, v51, v151
	v_min_u32_e32 v52, v52, v152
	v_min_u32_e32 v53, v53, v153
	v_max_u32_e32 v48, v154, v50
	v_max_u32_e32 v49, v134, v51
	v_max_u32_e32 v97, v143, v52
	v_max_u32_e32 v151, v149, v53
	v_max_u32_e32 v46, v48, v97
	v_max_u32_e32 v150, v49, v151
	v_min_u32_e32 v97, v48, v97
	v_min_u32_e32 v49, v49, v151
	v_min_u32_e32 v47, v46, v150
	v_max_u32_e32 v48, v97, v49
	v_min_u32_e32 v49, v97, v49
	v_cmp_lt_i32_e32 vcc, 0, v1
	s_and_saveexec_b64 s[0:1], vcc
	s_xor_b64 s[0:1], exec, s[0:1]
	s_cbranch_execz .LBB0_675
	s_nop 1
	v_ashrrev_i32_e32 v97, 31, v47
	v_bitop3_b32 v97, v47, v97, s12 bitop3:0x93
	v_add_f32_e32 v97, v54, v97
	v_cmp_lt_i32_e32 vcc, -1, v97
	s_nop 1
	v_cndmask_b32_e32 v151, -1, v132, vcc
	v_bitop3_b32 v97, v151, s60, v97 bitop3:0x48
	v_or_b32_e32 v97, 0xf6, v97
	v_cmp_ne_u32_e32 vcc, 1, v1
	s_and_saveexec_b64 s[4:5], vcc
	s_cbranch_execz .LBB0_674
	v_cmp_lt_i32_e32 vcc, -1, v49
	v_and_b32_e32 v97, 0xffffff80, v49
	v_and_b32_e32 v151, 0xffffff80, v48
	v_cndmask_b32_e64 v152, v132, -1, vcc
	v_cmp_lt_i32_e32 vcc, -1, v48
	v_xor_b32_e32 v153, v152, v97
	s_movk_i32 s6, 0xf4
	v_cndmask_b32_e64 v155, v132, -1, vcc
	v_xor_b32_e32 v152, v155, v151
	v_pk_add_f32 v[152:153], v[54:55], v[152:153] op_sel_hi:[0,1]
	v_cmp_lt_i32_e32 vcc, -1, v153
	v_and_b32_e32 v151, 0xffffff00, v153
	s_nop 0
	v_cndmask_b32_e32 v97, v133, v132, vcc
	v_cmp_lt_i32_e32 vcc, -1, v152
	v_bitop3_b32 v97, v97, s6, v151 bitop3:0xde
	v_and_b32_e32 v152, 0xffffff00, v152
	v_cndmask_b32_e32 v151, v133, v132, vcc
	s_movk_i32 s6, 0xf5
	v_bitop3_b32 v151, v151, s6, v152 bitop3:0xde
	v_cndmask_b32_e64 v97, v97, v151, s[38:39]

; __device__ __forceinline__ unsigned mono(float f) { const unsigned u = __float_as_uint(f); return (u & 0x80000000u) ? ~u : (u ^ 0x80000000u); }
; __device__ __forceinline__ float unmono(unsigned u) { return __uint_as_float((u & 0x80000000u) ? (u ^ 0x80000000u) : ~u); }
; __device__ __forceinline__ void topk_phase(LAS unsigned char* lds, const bf16_t* qp, const bf16_t* keys, const float* SU, const float* SV, int* sel_e, float* sel_g, float* sel_su, int G, int b) {
;     ...
;         float v1[16], v2[16];
; #pragma unroll
;         for (int i = 0; i < 16; ++i) { v1[i] = unmono(T[0][i] & ~127u); v2[i] = unmono(T[1][i] & ~127u); }
;         unsigned ck[16];
; #pragma unroll
;         for (int sidx = 0; sidx < 13; ++sidx) {
;             unsigned keyk[4];
; #pragma unroll
;             for (int k = 0; k < 4; ++k) {
;                 const int c = 4 * sidx + k;
;                 if (c < 50) { const int ci = cand_i(c), cj = cand_j(c); keyk[k] = (mono(v1[ci] + v2[cj]) & ~255u) | (unsigned)(255 - (ci * 16 + cj)); }
;                 else keyk[k] = 0u;
;             }
;             ck[sidx] = fq == 0 ? keyk[0] : fq == 1 ? keyk[1] : fq == 2 ? keyk[2] : keyk[3];
.LBB0_675:
	s_or_saveexec_b64 s[0:1], s[0:1]
	v_max_u32_e32 v46, v46, v150
	s_xor_b64 exec, exec, s[0:1]
	s_nop 1
	v_ashrrev_i32_e32 v97, 31, v46
	v_bitop3_b32 v97, v46, v97, s12 bitop3:0x93
	v_add_f32_e32 v97, v54, v97
	v_cmp_lt_i32_e32 vcc, -1, v97
	s_nop 1
	v_cndmask_b32_e32 v150, -1, v132, vcc
	v_bitop3_b32 v97, v150, s60, v97 bitop3:0x48
	v_or_b32_e32 v97, 0xf7, v97
	s_or_b64 exec, exec, s[0:1]
	v_min_u32_e32 v150, v154, v50
	v_min_u32_e32 v134, v134, v51
	v_min_u32_e32 v52, v143, v52
	v_min_u32_e32 v53, v149, v53
	v_max_u32_e32 v50, v150, v52
	v_max_u32_e32 v143, v134, v53
	v_min_u32_e32 v149, v150, v52
	v_min_u32_e32 v53, v134, v53
	v_min_u32_e32 v51, v50, v143
	v_max_u32_e32 v52, v149, v53
	v_min_u32_e32 v53, v149, v53
	v_cmp_lt_i32_e32 vcc, 0, v1
	s_and_saveexec_b64 s[0:1], vcc
	s_xor_b64 s[0:1], exec, s[0:1]
	s_cbranch_execz .LBB0_681
	s_nop 1
	v_ashrrev_i32_e32 v134, 31, v51
	v_bitop3_b32 v134, v51, v134, s12 bitop3:0x93
	v_add_f32_e32 v134, v54, v134
	v_cmp_lt_i32_e32 vcc, -1, v134
	s_nop 1
	v_cndmask_b32_e32 v149, -1, v132, vcc
	v_bitop3_b32 v134, v149, s60, v134 bitop3:0x48
	v_or_b32_e32 v134, 0xf2, v134
	v_cmp_ne_u32_e32 vcc, 1, v1
	s_and_saveexec_b64 s[4:5], vcc
	s_cbranch_execz .LBB0_680
	v_cmp_lt_i32_e32 vcc, -1, v53
	v_and_b32_e32 v134, 0xffffff80, v53
	v_and_b32_e32 v149, 0xffffff80, v52
	v_cndmask_b32_e64 v150, v132, -1, vcc
	v_cmp_lt_i32_e32 vcc, -1, v52
	v_xor_b32_e32 v151, v150, v134
	s_movk_i32 s6, 0xf0
	v_cndmask_b32_e64 v152, v132, -1, vcc
	v_xor_b32_e32 v150, v152, v149
	v_pk_add_f32 v[150:151], v[54:55], v[150:151] op_sel_hi:[0,1]
	v_cmp_lt_i32_e32 vcc, -1, v151
	v_and_b32_e32 v134, 0xffffff00, v151
	v_and_b32_e32 v149, 0xffffff00, v150
	v_cndmask_b32_e32 v54, v133, v132, vcc
	v_cmp_lt_i32_e32 vcc, -1, v150
	v_bitop3_b32 v54, v54, s6, v134 bitop3:0xde
	s_movk_i32 s6, 0xf1
	v_cndmask_b32_e32 v134, v133, v132, vcc
	v_bitop3_b32 v134, v134, s6, v149 bitop3:0xde
	v_cndmask_b32_e64 v134, v54, v134, s[38:39]

; __device__ __forceinline__ unsigned mono(float f) { const unsigned u = __float_as_uint(f); return (u & 0x80000000u) ? ~u : (u ^ 0x80000000u); }
; __device__ __forceinline__ float unmono(unsigned u) { return __uint_as_float((u & 0x80000000u) ? (u ^ 0x80000000u) : ~u); }
; __device__ __forceinline__ void topk_phase(LAS unsigned char* lds, const bf16_t* qp, const bf16_t* keys, const float* SU, const float* SV, int* sel_e, float* sel_g, float* sel_su, int G, int b) {
;     ...
;         float v1[16], v2[16];
; #pragma unroll
;         for (int i = 0; i < 16; ++i) { v1[i] = unmono(T[0][i] & ~127u); v2[i] = unmono(T[1][i] & ~127u); }
;         unsigned ck[16];
; #pragma unroll
;         for (int sidx = 0; sidx < 13; ++sidx) {
;             unsigned keyk[4];
; #pragma unroll
;             for (int k = 0; k < 4; ++k) {
;                 const int c = 4 * sidx + k;
;                 if (c < 50) { const int ci = cand_i(c), cj = cand_j(c); keyk[k] = (mono(v1[ci] + v2[cj]) & ~255u) | (unsigned)(255 - (ci * 16 + cj)); }
;                 else keyk[k] = 0u;
;             }
;             ck[sidx] = fq == 0 ? keyk[0] : fq == 1 ? keyk[1] : fq == 2 ? keyk[2] : keyk[3];
.LBB0_681:
	s_or_saveexec_b64 s[0:1], s[0:1]
	v_max_u32_e32 v50, v50, v143
	s_xor_b64 exec, exec, s[0:1]
	s_nop 1
	v_ashrrev_i32_e32 v134, 31, v50
	v_bitop3_b32 v134, v50, v134, s12 bitop3:0x93
	v_add_f32_e32 v54, v54, v134
	v_cmp_lt_i32_e32 vcc, -1, v54
	s_nop 1
	v_cndmask_b32_e32 v134, -1, v132, vcc
	v_bitop3_b32 v54, v134, s60, v54 bitop3:0x48
	v_or_b32_e32 v134, 0xf3, v54
	s_or_b64 exec, exec, s[0:1]
	v_min_u32_e32 v35, v35, v142
	v_cmp_lt_i32_e32 vcc, -1, v35
	s_nop 1
	v_cndmask_b32_e64 v54, v132, -1, vcc
	v_bitop3_b32 v54, v54, v35, s53 bitop3:0x78
	v_cmp_lt_i32_e32 vcc, 0, v1
	s_and_saveexec_b64 s[0:1], vcc
	s_xor_b64 s[0:1], exec, s[0:1]
	s_cbranch_execz .LBB0_687
	v_add_f32_e32 v142, v67, v54
	v_cmp_lt_i32_e32 vcc, -1, v142
	s_nop 1
	v_cndmask_b32_e32 v143, -1, v132, vcc
	v_bitop3_b32 v142, v143, s60, v142 bitop3:0x48
	v_or_b32_e32 v142, 0xee, v142
	v_cmp_ne_u32_e32 vcc, 1, v1
	s_and_saveexec_b64 s[4:5], vcc
	s_cbranch_execz .LBB0_686
	v_pk_add_f32 v[142:143], v[54:55], v[56:57] op_sel_hi:[0,1]
	v_cmp_lt_i32_e32 vcc, -1, v143
	v_and_b32_e32 v143, 0xffffff00, v143
	s_movk_i32 s6, 0xec
	v_cndmask_b32_e32 v149, v133, v132, vcc
	v_cmp_lt_i32_e32 vcc, -1, v142
	v_bitop3_b32 v143, v149, s6, v143 bitop3:0xde
	v_and_b32_e32 v142, 0xffffff00, v142
	v_cndmask_b32_e32 v149, v133, v132, vcc
	s_movk_i32 s6, 0xed
	v_bitop3_b32 v142, v149, s6, v142 bitop3:0xde
	v_cndmask_b32_e64 v142, v143, v142, s[38:39]

; __device__ __forceinline__ unsigned mono(float f) { const unsigned u = __float_as_uint(f); return (u & 0x80000000u) ? ~u : (u ^ 0x80000000u); }
; __device__ __forceinline__ float unmono(unsigned u) { return __uint_as_float((u & 0x80000000u) ? (u ^ 0x80000000u) : ~u); }
; __device__ __forceinline__ void topk_phase(LAS unsigned char* lds, const bf16_t* qp, const bf16_t* keys, const float* SU, const float* SV, int* sel_e, float* sel_g, float* sel_su, int G, int b) {
;     ...
;         float v1[16], v2[16];
; #pragma unroll
;         for (int i = 0; i < 16; ++i) { v1[i] = unmono(T[0][i] & ~127u); v2[i] = unmono(T[1][i] & ~127u); }
;         unsigned ck[16];
; #pragma unroll
;         for (int sidx = 0; sidx < 13; ++sidx) {
;             unsigned keyk[4];
; #pragma unroll
;             for (int k = 0; k < 4; ++k) {
;                 const int c = 4 * sidx + k;
;                 if (c < 50) { const int ci = cand_i(c), cj = cand_j(c); keyk[k] = (mono(v1[ci] + v2[cj]) & ~255u) | (unsigned)(255 - (ci * 16 + cj)); }
;                 else keyk[k] = 0u;
;             }
;             ck[sidx] = fq == 0 ? keyk[0] : fq == 1 ? keyk[1] : fq == 2 ? keyk[2] : keyk[3];
.LBB0_705:
	s_andn2_saveexec_b64 s[0:1], s[0:1]
	v_add_f32_e32 v54, v54, v147
	v_cmp_lt_i32_e32 vcc, -1, v54
	s_nop 1
	v_cndmask_b32_e32 v145, -1, v132, vcc
	v_bitop3_b32 v54, v145, s60, v54 bitop3:0x48
	v_or_b32_e32 v145, 0xdb, v54
	s_or_b64 exec, exec, s[0:1]
	v_min_u32_e32 v138, v55, v138
	v_min_u32_e32 v139, v135, v139
	v_min_u32_e32 v136, v136, v140
	v_min_u32_e32 v137, v137, v141
	v_max_u32_e32 v55, v138, v136
	v_max_u32_e32 v140, v139, v137
	v_max_u32_e32 v54, v55, v140
	v_cmp_lt_i32_e32 vcc, 0, v1
	s_and_saveexec_b64 s[0:1], vcc
	s_xor_b64 s[0:1], exec, s[0:1]
	s_cbranch_execz .LBB0_711
	s_nop 1
	v_ashrrev_i32_e32 v58, 31, v54
	v_bitop3_b32 v58, v54, v58, s12 bitop3:0x93
	v_add_f32_e32 v135, v66, v58
	v_cmp_lt_i32_e32 vcc, -1, v135
	s_nop 1
	v_cndmask_b32_e32 v141, -1, v132, vcc
	v_bitop3_b32 v135, v141, s60, v135 bitop3:0x48
	v_or_b32_e32 v135, 0xbf, v135
	v_cmp_ne_u32_e32 vcc, 1, v1
	s_and_saveexec_b64 s[4:5], vcc
	s_cbranch_execz .LBB0_710
	v_pk_mov_b32 v[56:57], v[66:67], v[56:57] op_sel:[1,0]
	s_movk_i32 s6, 0xbd
	v_pk_add_f32 v[56:57], v[58:59], v[56:57] op_sel_hi:[0,1]
	v_cmp_lt_i32_e32 vcc, -1, v57
	v_and_b32_e32 v57, 0xffffff00, v57
	s_nop 0
	v_cndmask_b32_e32 v58, v133, v132, vcc
	v_cmp_lt_i32_e32 vcc, -1, v56
	v_bitop3_b32 v57, v58, s6, v57 bitop3:0xde
	v_and_b32_e32 v56, 0xffffff00, v56
	v_cndmask_b32_e32 v58, v133, v132, vcc
	s_movk_i32 s6, 0xbe
	v_bitop3_b32 v56, v58, s6, v56 bitop3:0xde
	v_cndmask_b32_e64 v135, v57, v56, s[38:39]

; __device__ __forceinline__ unsigned mono(float f) { const unsigned u = __float_as_uint(f); return (u & 0x80000000u) ? ~u : (u ^ 0x80000000u); }
; __device__ __forceinline__ float unmono(unsigned u) { return __uint_as_float((u & 0x80000000u) ? (u ^ 0x80000000u) : ~u); }
; __device__ __forceinline__ void topk_phase(LAS unsigned char* lds, const bf16_t* qp, const bf16_t* keys, const float* SU, const float* SV, int* sel_e, float* sel_g, float* sel_su, int G, int b) {
;     ...
;         float v1[16], v2[16];
; #pragma unroll
;         for (int i = 0; i < 16; ++i) { v1[i] = unmono(T[0][i] & ~127u); v2[i] = unmono(T[1][i] & ~127u); }
;         unsigned ck[16];
; #pragma unroll
;         for (int sidx = 0; sidx < 13; ++sidx) {
;             unsigned keyk[4];
; #pragma unroll
;             for (int k = 0; k < 4; ++k) {
;                 const int c = 4 * sidx + k;
;                 if (c < 50) { const int ci = cand_i(c), cj = cand_j(c); keyk[k] = (mono(v1[ci] + v2[cj]) & ~255u) | (unsigned)(255 - (ci * 16 + cj)); }
;                 else keyk[k] = 0u;
;             }
;             ck[sidx] = fq == 0 ? keyk[0] : fq == 1 ? keyk[1] : fq == 2 ? keyk[2] : keyk[3];
.LBB0_711:
	s_andn2_saveexec_b64 s[0:1], s[0:1]
	v_add_f32_e32 v56, v57, v58
	v_cmp_lt_i32_e32 vcc, -1, v56
	s_nop 1
	v_cndmask_b32_e32 v57, -1, v132, vcc
	v_bitop3_b32 v56, v57, s60, v56 bitop3:0x48
	v_or_b32_e32 v135, 0xcc, v56
	s_or_b64 exec, exec, s[0:1]
	v_min_u32_e32 v55, v55, v140
	v_min_u32_e32 v57, v138, v136
	v_min_u32_e32 v58, v139, v137
	v_ashrrev_i32_e32 v56, 31, v55
	v_bitop3_b32 v140, v55, v56, s12 bitop3:0x93
	v_max_u32_e32 v56, v57, v58
	v_cmp_lt_i32_e32 vcc, 0, v1
	s_and_saveexec_b64 s[0:1], vcc
	s_xor_b64 s[0:1], exec, s[0:1]
	s_cbranch_execz .LBB0_717
	v_add_f32_e32 v136, v67, v140
	v_cmp_lt_i32_e32 vcc, -1, v136
	s_nop 1
	v_cndmask_b32_e32 v137, -1, v132, vcc
	v_bitop3_b32 v136, v137, s60, v136 bitop3:0x48
	v_or_b32_e32 v136, 0xae, v136
	v_cmp_ne_u32_e32 vcc, 1, v1
	s_and_saveexec_b64 s[4:5], vcc
	s_cbranch_execz .LBB0_716
	s_movk_i32 s6, 0x9e
	s_nop 0
	v_ashrrev_i32_e32 v136, 31, v56
	v_bitop3_b32 v136, v56, v136, s12 bitop3:0x93
	v_pk_add_f32 v[136:137], v[136:137], v[66:67] op_sel_hi:[0,1]
	v_cmp_lt_i32_e32 vcc, -1, v137
	v_and_b32_e32 v137, 0xffffff00, v137
	s_nop 0
	v_cndmask_b32_e32 v138, v133, v132, vcc
	v_cmp_lt_i32_e32 vcc, -1, v136
	v_bitop3_b32 v137, v138, s6, v137 bitop3:0xde
	v_and_b32_e32 v136, 0xffffff00, v136
	v_cndmask_b32_e32 v138, v133, v132, vcc
	s_movk_i32 s6, 0x9f
	v_bitop3_b32 v136, v138, s6, v136 bitop3:0xde
	v_cndmask_b32_e64 v136, v137, v136, s[38:39]

; __device__ __forceinline__ unsigned mono(float f) { const unsigned u = __float_as_uint(f); return (u & 0x80000000u) ? ~u : (u ^ 0x80000000u); }
; __device__ __forceinline__ float unmono(unsigned u) { return __uint_as_float((u & 0x80000000u) ? (u ^ 0x80000000u) : ~u); }
; __device__ __forceinline__ void topk_phase(LAS unsigned char* lds, const bf16_t* qp, const bf16_t* keys, const float* SU, const float* SV, int* sel_e, float* sel_g, float* sel_su, int G, int b) {
;     ...
;         float v1[16], v2[16];
; #pragma unroll
;         for (int i = 0; i < 16; ++i) { v1[i] = unmono(T[0][i] & ~127u); v2[i] = unmono(T[1][i] & ~127u); }
;         unsigned ck[16];
; #pragma unroll
;         for (int sidx = 0; sidx < 13; ++sidx) {
;             unsigned keyk[4];
; #pragma unroll
;             for (int k = 0; k < 4; ++k) {
;                 const int c = 4 * sidx + k;
;                 if (c < 50) { const int ci = cand_i(c), cj = cand_j(c); keyk[k] = (mono(v1[ci] + v2[cj]) & ~255u) | (unsigned)(255 - (ci * 16 + cj)); }
;                 else keyk[k] = 0u;
;             }
;             ck[sidx] = fq == 0 ? keyk[0] : fq == 1 ? keyk[1] : fq == 2 ? keyk[2] : keyk[3];
.LBB0_717:
	s_andn2_saveexec_b64 s[0:1], s[0:1]
	v_add_f32_e32 v136, v66, v140
	v_cmp_lt_i32_e32 vcc, -1, v136
	s_nop 1
	v_cndmask_b32_e32 v137, -1, v132, vcc
	v_bitop3_b32 v136, v137, s60, v136 bitop3:0x48
	v_or_b32_e32 v136, 0xaf, v136
	s_or_b64 exec, exec, s[0:1]
	v_min_u32_e32 v57, v57, v58
	v_min_u32_e32 v71, v59, v71
	v_min_u32_e32 v60, v60, v72
	v_min_u32_e32 v72, v61, v73
	v_min_u32_e32 v62, v62, v74
	v_min_u32_e32 v63, v63, v75
	v_min_u32_e32 v64, v64, v76
	v_min_u32_e32 v65, v65, v77
	v_min_u32_e32 v73, v70, v96
	v_max_u32_e32 v61, v71, v63
	v_max_u32_e32 v74, v60, v64
	v_max_u32_e32 v75, v72, v65
	v_max_u32_e32 v76, v62, v73
	v_ashrrev_i32_e32 v58, 31, v57
	v_max_u32_e32 v59, v61, v75
	v_max_u32_e32 v70, v74, v76
	v_bitop3_b32 v137, v57, v58, s12 bitop3:0x93
	v_max_u32_e32 v58, v59, v70
	v_min_u32_e32 v59, v59, v70
	v_cmp_lt_i32_e32 vcc, 0, v1
	s_and_saveexec_b64 s[0:1], vcc
	s_xor_b64 s[0:1], exec, s[0:1]
	s_cbranch_execz .LBB0_723
	v_add_f32_e32 v70, v67, v137
	v_cmp_lt_i32_e32 vcc, -1, v70
	s_nop 1
	v_cndmask_b32_e32 v77, -1, v132, vcc
	v_bitop3_b32 v70, v77, s60, v70 bitop3:0x48
	v_or_b32_e32 v70, 0x8e, v70
	v_cmp_ne_u32_e32 vcc, 1, v1
	s_and_saveexec_b64 s[4:5], vcc
	s_cbranch_execz .LBB0_722
	v_cmp_lt_i32_e32 vcc, -1, v59
	v_and_b32_e32 v70, 0xffffff80, v59
	v_and_b32_e32 v77, 0xffffff80, v58
	v_cndmask_b32_e64 v96, v132, -1, vcc
	v_cmp_lt_i32_e32 vcc, -1, v58
	v_xor_b32_e32 v139, v96, v70
	s_movk_i32 s6, 0x6f
	v_cndmask_b32_e64 v137, v132, -1, vcc
	v_xor_b32_e32 v138, v137, v77
	v_pk_add_f32 v[138:139], v[66:67], v[138:139] op_sel_hi:[0,1]
	v_cmp_lt_i32_e32 vcc, -1, v139
	v_and_b32_e32 v77, 0xffffff00, v139
	v_and_b32_e32 v96, 0xffffff00, v138
	v_cndmask_b32_e32 v70, v133, v132, vcc
	v_cmp_lt_i32_e32 vcc, -1, v138
	v_bitop3_b32 v70, v70, s6, v77 bitop3:0xde
	s_movk_i32 s6, 0x7f
	v_cndmask_b32_e32 v77, v133, v132, vcc
	v_bitop3_b32 v77, v77, s6, v96 bitop3:0xde
	v_cndmask_b32_e64 v70, v70, v77, s[38:39]

; __device__ __forceinline__ unsigned mono(float f) { const unsigned u = __float_as_uint(f); return (u & 0x80000000u) ? ~u : (u ^ 0x80000000u); }
; __device__ __forceinline__ float unmono(unsigned u) { return __uint_as_float((u & 0x80000000u) ? (u ^ 0x80000000u) : ~u); }
; __device__ __forceinline__ void topk_phase(LAS unsigned char* lds, const bf16_t* qp, const bf16_t* keys, const float* SU, const float* SV, int* sel_e, float* sel_g, float* sel_su, int G, int b) {
;     ...
;         float v1[16], v2[16];
; #pragma unroll
;         for (int i = 0; i < 16; ++i) { v1[i] = unmono(T[0][i] & ~127u); v2[i] = unmono(T[1][i] & ~127u); }
;         unsigned ck[16];
; #pragma unroll
;         for (int sidx = 0; sidx < 13; ++sidx) {
;             unsigned keyk[4];
; #pragma unroll
;             for (int k = 0; k < 4; ++k) {
;                 const int c = 4 * sidx + k;
;                 if (c < 50) { const int ci = cand_i(c), cj = cand_j(c); keyk[k] = (mono(v1[ci] + v2[cj]) & ~255u) | (unsigned)(255 - (ci * 16 + cj)); }
;                 else keyk[k] = 0u;
;             }
;             ck[sidx] = fq == 0 ? keyk[0] : fq == 1 ? keyk[1] : fq == 2 ? keyk[2] : keyk[3];
.LBB0_723:
	s_andn2_saveexec_b64 s[0:1], s[0:1]
	v_add_f32_e32 v70, v66, v137
	v_cmp_lt_i32_e32 vcc, -1, v70
	s_nop 1
	v_cndmask_b32_e32 v77, -1, v132, vcc
	v_bitop3_b32 v70, v77, s60, v70 bitop3:0x48
	v_or_b32_e32 v70, 0x8f, v70
	s_or_b64 exec, exec, s[0:1]
	v_min_u32_e32 v76, v74, v76
	v_min_u32_e32 v74, v71, v63
	v_min_u32_e32 v64, v60, v64
	v_min_u32_e32 v65, v72, v65
	v_min_u32_e32 v72, v62, v73
	v_min_u32_e32 v75, v61, v75
	v_max_u32_e32 v60, v74, v65
	v_max_u32_e32 v63, v64, v72
	v_min_u32_e32 v61, v75, v76
	v_max_u32_e32 v62, v60, v63
	v_min_u32_e32 v63, v60, v63
	v_cmp_lt_i32_e32 vcc, 0, v1
	s_and_saveexec_b64 s[0:1], vcc
	s_xor_b64 s[0:1], exec, s[0:1]
	s_cbranch_execz .LBB0_729
	s_nop 1
	v_ashrrev_i32_e32 v60, 31, v61
	v_bitop3_b32 v60, v61, v60, s12 bitop3:0x93
	v_add_f32_e32 v60, v66, v60
	v_cmp_lt_i32_e32 vcc, -1, v60
	s_nop 1
	v_cndmask_b32_e32 v71, -1, v132, vcc
	v_bitop3_b32 v60, v71, s60, v60 bitop3:0x48
	v_or_b32_e32 v71, 0x4f, v60
	v_cmp_ne_u32_e32 vcc, 1, v1
	s_and_saveexec_b64 s[4:5], vcc
	s_cbranch_execz .LBB0_728
	v_cmp_lt_i32_e32 vcc, -1, v63
	v_and_b32_e32 v60, 0xffffff80, v63
	v_and_b32_e32 v71, 0xffffff80, v62
	v_cndmask_b32_e64 v73, v132, -1, vcc
	v_cmp_lt_i32_e32 vcc, -1, v62
	v_xor_b32_e32 v139, v73, v60
	s_nop 0
	v_cndmask_b32_e64 v77, v132, -1, vcc
	v_xor_b32_e32 v138, v77, v71
	v_pk_add_f32 v[138:139], v[66:67], v[138:139] op_sel_hi:[0,1]
	v_cmp_lt_i32_e32 vcc, -1, v139
	v_and_b32_e32 v67, 0xffffff00, v139
	v_and_b32_e32 v71, 0xffffff00, v138
	v_cndmask_b32_e32 v60, v133, v132, vcc
	v_cmp_lt_i32_e32 vcc, -1, v138
	v_bitop3_b32 v60, v60, 47, v67 bitop3:0xde
	s_nop 0
	v_cndmask_b32_e32 v67, v133, v132, vcc
	v_bitop3_b32 v67, v67, 63, v71 bitop3:0xde
	v_cndmask_b32_e64 v71, v60, v67, s[38:39]

; __device__ __forceinline__ unsigned mono(float f) { const unsigned u = __float_as_uint(f); return (u & 0x80000000u) ? ~u : (u ^ 0x80000000u); }
; __device__ __forceinline__ float unmono(unsigned u) { return __uint_as_float((u & 0x80000000u) ? (u ^ 0x80000000u) : ~u); }
; __device__ __forceinline__ void topk_phase(LAS unsigned char* lds, const bf16_t* qp, const bf16_t* keys, const float* SU, const float* SV, int* sel_e, float* sel_g, float* sel_su, int G, int b) {
;     ...
;         for (int i = 0; i < 16; ++i) { v1[i] = unmono(T[0][i] & ~127u); v2[i] = unmono(T[1][i] & ~127u); }
;         unsigned ck[16];
; #pragma unroll
;         for (int sidx = 0; sidx < 13; ++sidx) {
;             unsigned keyk[4];
; #pragma unroll
;             for (int k = 0; k < 4; ++k) {
;                 const int c = 4 * sidx + k;
;                 if (c < 50) { const int ci = cand_i(c), cj = cand_j(c); keyk[k] = (mono(v1[ci] + v2[cj]) & ~255u) | (unsigned)(255 - (ci * 16 + cj)); }
;                 else keyk[k] = 0u;
;             }
;             ck[sidx] = fq == 0 ? keyk[0] : fq == 1 ? keyk[1] : fq == 2 ? keyk[2] : keyk[3];
;         }
;         ck[13] = 0u; ck[14] = 0u; ck[15] = 0u;
;         SN_SORT16(ck);
;         TOPK_XMERGE(ck, 16); TOPK_XMERGE(ck, 32);
.LBB0_729:
	s_or_saveexec_b64 s[0:1], s[0:1]
	v_max_u32_e32 v60, v75, v76
	s_xor_b64 exec, exec, s[0:1]
	s_nop 1
	v_ashrrev_i32_e32 v67, 31, v60
	v_bitop3_b32 v67, v60, v67, s12 bitop3:0x93
	v_add_f32_e32 v67, v66, v67
	v_cmp_lt_i32_e32 vcc, -1, v67
	s_nop 1
	v_cndmask_b32_e32 v71, -1, v132, vcc
	v_bitop3_b32 v67, v71, s60, v67 bitop3:0x48
	v_or_b32_e32 v71, 0x5f, v67
	s_or_b64 exec, exec, s[0:1]
	v_min_u32_e32 v73, v74, v65
	v_min_u32_e32 v64, v64, v72
	v_min_u32_e32 v65, v73, v64
	v_cmp_lt_i32_e32 vcc, 0, v1
	s_and_saveexec_b64 s[0:1], vcc
	s_xor_b64 s[0:1], exec, s[0:1]
	s_cbranch_execz .LBB0_735
	s_nop 1
	v_ashrrev_i32_e32 v67, 31, v65
	v_bitop3_b32 v67, v65, v67, s12 bitop3:0x93
	v_add_f32_e32 v66, v66, v67
	v_cmp_lt_i32_e32 vcc, -1, v66
	s_nop 1
	v_cndmask_b32_e32 v67, -1, v132, vcc
	v_xor_b32_e32 v66, v67, v66
	v_and_or_b32 v67, v66, s60, 15
	v_cmp_ne_u32_e32 vcc, 1, v1
	s_and_saveexec_b64 s[4:5], vcc
	v_mov_b32_e32 v67, 0
	s_or_b64 exec, exec, s[4:5]
.LBB0_735:
	s_or_saveexec_b64 s[0:1], s[0:1]
	v_max_u32_e32 v64, v73, v64
	s_xor_b64 exec, exec, s[0:1]
	s_nop 1
	v_ashrrev_i32_e32 v67, 31, v64
	v_bitop3_b32 v67, v64, v67, s12 bitop3:0x93
	v_add_f32_e32 v66, v66, v67
	v_cmp_lt_i32_e32 vcc, -1, v66
	s_nop 1
	v_cndmask_b32_e32 v67, -1, v132, vcc
	v_xor_b32_e32 v66, v67, v66
	v_and_or_b32 v67, v66, s60, 31
	s_or_b64 exec, exec, s[0:1]
	v_max_u32_e32 v66, v68, v69
	v_min_u32_e32 v68, v68, v69
	v_max_u32_e32 v69, v97, v134
	v_min_u32_e32 v72, v97, v134
	v_max_u32_e32 v73, v66, v69
	v_min_u32_e32 v66, v66, v69
	v_max_u32_e32 v69, v68, v72
	v_min_u32_e32 v68, v68, v72
	v_max_u32_e32 v72, v69, v66
	v_min_u32_e32 v66, v69, v66
	v_max_u32_e32 v69, v142, v143
	v_min_u32_e32 v74, v142, v143
	v_max_u32_e32 v75, v144, v145
	v_min_u32_e32 v76, v144, v145
	v_max_u32_e32 v77, v69, v75
	v_min_u32_e32 v69, v69, v75
	v_max_u32_e32 v75, v74, v76
	v_min_u32_e32 v74, v74, v76
	v_max_u32_e32 v76, v75, v69
	v_min_u32_e32 v69, v75, v69
	v_max_u32_e32 v75, v73, v77
	v_min_u32_e32 v73, v73, v77
	v_max_u32_e32 v77, v66, v69
	v_min_u32_e32 v66, v66, v69
	v_max_u32_e32 v69, v77, v73
	v_min_u32_e32 v73, v77, v73
	v_max_u32_e32 v77, v72, v76
	v_min_u32_e32 v72, v72, v76
	v_max_u32_e32 v76, v68, v74
	v_min_u32_e32 v68, v68, v74
	v_max_u32_e32 v74, v76, v72
	v_min_u32_e32 v72, v76, v72
	v_max_u32_e32 v76, v77, v69
	v_min_u32_e32 v69, v77, v69
	v_max_u32_e32 v77, v74, v73
	v_min_u32_e32 v73, v74, v73
	v_max_u32_e32 v74, v72, v66
	v_min_u32_e32 v66, v72, v66
	v_max_u32_e32 v72, v135, v136
	v_min_u32_e32 v96, v135, v136
	v_max_u32_e32 v97, v70, v71
	v_min_u32_e32 v70, v70, v71
	v_max_u32_e32 v71, v72, v97
	v_min_u32_e32 v72, v72, v97
	v_max_u32_e32 v97, v96, v70
	v_min_u32_e32 v134, v97, v72
	v_max_u32_e32 v135, v71, v67
	v_min_u32_e32 v67, v71, v67
	v_min_u32_e32 v70, v96, v70
	v_max_u32_e32 v71, v134, v67
	v_min_u32_e32 v134, v134, v67
	v_max_u32_e32 v96, v97, v72
	v_med3_u32 v67, v97, v72, v67
	v_max_u32_e32 v72, v70, v134
	v_min_u32_e32 v70, v70, v134
	v_max_u32_e32 v71, v96, v71
	v_max_u32_e32 v96, v75, v135
	v_min_u32_e32 v75, v75, v135
	v_max_u32_e32 v97, v73, v70
	v_min_u32_e32 v70, v73, v70
	v_max_u32_e32 v73, v97, v75
	v_min_u32_e32 v75, v97, v75
	v_max_u32_e32 v97, v69, v67
	v_min_u32_e32 v67, v69, v67
	v_max_u32_e32 v69, v66, v67
	v_min_u32_e32 v66, v66, v67
	v_max_u32_e32 v67, v97, v73
	v_min_u32_e32 v73, v97, v73
	v_max_u32_e32 v97, v69, v75
	v_min_u32_e32 v69, v69, v75
	v_max_u32_e32 v75, v66, v70
	v_min_u32_e32 v66, v66, v70
	v_max_u32_e32 v70, v76, v71
	v_min_u32_e32 v71, v76, v71
	v_max_u32_e32 v76, v74, v71
	v_min_u32_e32 v71, v74, v71
	v_max_u32_e32 v74, v77, v72
	v_min_u32_e32 v72, v77, v72
	v_max_u32_e32 v77, v68, v72
	v_min_u32_e32 v68, v68, v72
	v_max_u32_e32 v72, v74, v76
	v_min_u32_e32 v74, v74, v76
	v_max_u32_e32 v76, v77, v71
	v_min_u32_e32 v71, v77, v71
	v_max_u32_e32 v77, v70, v67
	v_min_u32_e32 v67, v70, v67
	v_max_u32_e32 v70, v72, v73
	v_min_u32_e32 v72, v72, v73
	v_max_u32_e32 v73, v74, v97
	v_min_u32_e32 v74, v74, v97
	v_max_u32_e32 v97, v76, v69
	v_min_u32_e32 v69, v76, v69
	v_max_u32_e32 v76, v71, v75
	v_min_u32_e32 v71, v71, v75
	v_max_u32_e32 v75, v68, v66
	v_min_u32_e32 v66, v68, v66
	v_mov_b32_e32 v68, v96
	v_mov_b32_e32 v134, v77
	v_mov_b32_e32 v135, v67
	v_mov_b32_e32 v136, v70
	v_mov_b32_e32 v137, v72
	v_mov_b32_e32 v138, v73
	v_mov_b32_e32 v139, v74
	v_mov_b32_e32 v140, v97
	v_mov_b32_e32 v141, v69
	v_mov_b32_e32 v142, v76
	v_mov_b32_e32 v143, v71
	v_mov_b32_e32 v144, v75
	v_mov_b32_e32 v145, v66
	v_mov_b32_e32 v146, 0
	v_mov_b32_e32 v147, 0
	v_permlane16_swap_b32_e32 v96, v68
	v_permlane16_swap_b32_e32 v77, v134
	v_permlane16_swap_b32_e32 v67, v135
	v_permlane16_swap_b32_e32 v70, v136
	v_permlane16_swap_b32_e32 v72, v137
	v_permlane16_swap_b32_e32 v73, v138
	v_permlane16_swap_b32_e32 v74, v139
	v_permlane16_swap_b32_e32 v97, v140
	v_permlane16_swap_b32_e32 v69, v141
	v_permlane16_swap_b32_e32 v76, v142
	v_permlane16_swap_b32_e32 v71, v143
	v_permlane16_swap_b32_e32 v75, v144
	v_permlane16_swap_b32_e32 v66, v145
	v_permlane16_swap_b32_e32 v146, v147
	v_max_u32_e32 v96, v96, v147
	v_max_u32_e32 v77, v77, v147
	v_max_u32_e32 v67, v67, v147
	v_max_u32_e32 v70, v70, v145
	v_max_u32_e32 v72, v72, v144
	v_max_u32_e32 v73, v73, v143
	v_max_u32_e32 v74, v74, v142
	v_max_u32_e32 v97, v97, v141
	v_max_u32_e32 v69, v69, v140
	v_max_u32_e32 v76, v76, v139
	v_max_u32_e32 v71, v71, v138
	v_max_u32_e32 v75, v75, v137
	v_max_u32_e32 v66, v66, v136
	v_max_u32_e32 v135, v146, v135
	v_max_u32_e32 v134, v146, v134
	v_max_u32_e32 v68, v146, v68
	v_max_u32_e32 v136, v96, v69
	v_min_u32_e32 v69, v96, v69
	v_max_u32_e32 v96, v77, v76
; __device__ __forceinline__ float unmono(unsigned u) { return __uint_as_float((u & 0x80000000u) ? (u ^ 0x80000000u) : ~u); }
; __device__ __forceinline__ void topk_phase(LAS unsigned char* lds, const bf16_t* qp, const bf16_t* keys, const float* SU, const float* SV, int* sel_e, float* sel_g, float* sel_su, int G, int b) {
;     ...
;         SN_SORT16(ck);
;         TOPK_XMERGE(ck, 16); TOPK_XMERGE(ck, 32);
;         if (fq == 0) {
; #pragma unroll
;             for (int i = 0; i < 16; ++i) { wl[i] = T[0][i]; wl[16 + i] = T[1][i]; }
;         }
;         asm volatile("" ::: "memory");
;         {
;             const float vmax = unmono(ck[0] & ~255u);
;             float esum = 0.f;
; #pragma unroll
;             for (int k = 0; k < 16; ++k) esum += __expf(unmono(ck[k] & ~255u) - vmax);
	v_min_u32_e32 v76, v77, v76
	v_max_u32_e32 v77, v67, v71
	v_min_u32_e32 v67, v67, v71
	v_max_u32_e32 v71, v70, v75
	v_min_u32_e32 v70, v70, v75
	v_max_u32_e32 v75, v72, v66
	v_min_u32_e32 v66, v72, v66
	v_max_u32_e32 v72, v73, v135
	v_min_u32_e32 v73, v73, v135
	v_max_u32_e32 v135, v74, v134
	v_min_u32_e32 v74, v74, v134
	v_max_u32_e32 v134, v97, v68
	v_min_u32_e32 v68, v97, v68
	v_max_u32_e32 v97, v136, v75
	v_min_u32_e32 v75, v136, v75
	v_max_u32_e32 v136, v96, v72
	v_min_u32_e32 v72, v96, v72
	v_max_u32_e32 v96, v77, v135
	v_min_u32_e32 v77, v77, v135
	v_max_u32_e32 v135, v71, v134
	v_min_u32_e32 v71, v71, v134
	v_max_u32_e32 v134, v69, v66
	v_min_u32_e32 v66, v69, v66
	v_max_u32_e32 v69, v76, v73
	v_min_u32_e32 v73, v76, v73
	v_max_u32_e32 v76, v67, v74
	v_min_u32_e32 v67, v67, v74
	v_max_u32_e32 v74, v70, v68
	v_min_u32_e32 v68, v70, v68
	v_max_u32_e32 v70, v97, v96
	v_min_u32_e32 v96, v97, v96
	v_max_u32_e32 v97, v136, v135
	v_min_u32_e32 v135, v136, v135
	v_max_u32_e32 v136, v75, v77
	v_min_u32_e32 v75, v75, v77
	v_max_u32_e32 v77, v72, v71
	v_min_u32_e32 v137, v72, v71
	v_max_u32_e32 v138, v134, v76
	v_min_u32_e32 v134, v134, v76
	v_max_u32_e32 v76, v69, v74
	v_min_u32_e32 v139, v69, v74
	v_max_u32_e32 v140, v66, v67
	v_min_u32_e32 v141, v66, v67
	v_max_u32_e32 v142, v73, v68
	v_min_u32_e32 v143, v73, v68
	v_max_u32_e32 v66, v70, v97
	v_min_u32_e32 v67, v70, v97
	v_max_u32_e32 v68, v96, v135
	v_min_u32_e32 v69, v96, v135
	v_max_u32_e32 v70, v136, v77
	v_min_u32_e32 v71, v136, v77
	v_max_u32_e32 v72, v75, v137
	v_min_u32_e32 v73, v75, v137
	v_max_u32_e32 v74, v138, v76
	v_min_u32_e32 v75, v138, v76
	v_max_u32_e32 v76, v134, v139
	v_min_u32_e32 v77, v134, v139
	v_max_u32_e32 v96, v140, v142
	v_min_u32_e32 v97, v140, v142
	v_max_u32_e32 v134, v141, v143
	v_min_u32_e32 v135, v141, v143
	v_mov_b32_e32 v136, v66
	v_mov_b32_e32 v137, v67
	v_mov_b32_e32 v138, v68
	v_mov_b32_e32 v139, v69
	v_mov_b32_e32 v140, v70
	v_mov_b32_e32 v141, v71
	v_mov_b32_e32 v142, v72
	v_mov_b32_e32 v143, v73
	v_mov_b32_e32 v144, v74
	v_mov_b32_e32 v145, v75
	v_mov_b32_e32 v146, v76
	v_mov_b32_e32 v147, v77
	v_mov_b32_e32 v148, v96
	v_mov_b32_e32 v149, v97
	v_mov_b32_e32 v150, v134
	v_mov_b32_e32 v151, v135
	v_permlane32_swap_b32_e32 v66, v136
	v_permlane32_swap_b32_e32 v67, v137
	v_permlane32_swap_b32_e32 v68, v138
	v_permlane32_swap_b32_e32 v69, v139
	v_permlane32_swap_b32_e32 v70, v140
	v_permlane32_swap_b32_e32 v71, v141
	v_permlane32_swap_b32_e32 v72, v142
	v_permlane32_swap_b32_e32 v73, v143
	v_permlane32_swap_b32_e32 v74, v144
	v_permlane32_swap_b32_e32 v75, v145
	v_permlane32_swap_b32_e32 v76, v146
	v_permlane32_swap_b32_e32 v77, v147
	v_permlane32_swap_b32_e32 v96, v148
	v_permlane32_swap_b32_e32 v97, v149
	v_permlane32_swap_b32_e32 v134, v150
	v_permlane32_swap_b32_e32 v135, v151
	s_and_saveexec_b64 s[0:1], s[40:41]
	s_cbranch_execz .LBB0_739
	ds_write_b128 v83, v[34:37]
	ds_write_b128 v83, v[38:41] offset:64
	ds_write_b128 v83, v[54:57] offset:16
	ds_write_b128 v83, v[42:45] offset:80
	ds_write_b128 v83, v[58:61] offset:32
	ds_write_b128 v83, v[46:49] offset:96
	ds_write_b128 v83, v[62:65] offset:48
	ds_write_b128 v83, v[50:53] offset:112
.LBB0_739:
	s_or_b64 exec, exec, s[0:1]
	v_max_u32_e32 v34, v66, v151
	v_max_u32_e32 v35, v67, v150
	v_max_u32_e32 v36, v68, v149
	v_max_u32_e32 v37, v69, v148
	v_max_u32_e32 v38, v70, v147
	v_max_u32_e32 v39, v71, v146
	v_max_u32_e32 v40, v72, v145
	v_max_u32_e32 v41, v73, v144
	v_max_u32_e32 v42, v74, v143
	v_max_u32_e32 v43, v75, v142
	v_max_u32_e32 v44, v76, v141
	v_max_u32_e32 v45, v77, v140
	v_max_u32_e32 v46, v96, v139
	v_max_u32_e32 v47, v97, v138
	v_max_u32_e32 v48, v134, v137
	v_max_u32_e32 v49, v135, v136
	v_max_u32_e32 v50, v34, v42
	v_min_u32_e32 v34, v34, v42
	v_max_u32_e32 v42, v35, v43
	v_min_u32_e32 v35, v35, v43
	v_max_u32_e32 v43, v36, v44
	v_min_u32_e32 v36, v36, v44
	v_max_u32_e32 v44, v37, v45
	v_min_u32_e32 v37, v37, v45
	v_max_u32_e32 v45, v38, v46
	v_min_u32_e32 v51, v38, v46
	v_max_u32_e32 v46, v39, v47
	v_min_u32_e32 v52, v39, v47
	v_max_u32_e32 v47, v40, v48
	v_min_u32_e32 v53, v40, v48
	v_max_u32_e32 v48, v41, v49
	v_min_u32_e32 v55, v41, v49
	v_max_u32_e32 v39, v50, v45
	v_min_u32_e32 v38, v50, v45
	v_max_u32_e32 v41, v42, v46
	v_max_u32_e32 v45, v43, v47
	v_max_u32_e32 v49, v44, v48
	v_max_u32_e32 v59, v39, v45
	v_max_u32_e32 v62, v41, v49
	v_max_u32_e32 v56, v36, v53
	v_min_u32_e32 v54, v36, v53
	v_max_u32_e32 v36, v59, v62
	v_min_u32_e32 v40, v42, v46
	v_min_u32_e32 v42, v43, v47
	v_min_u32_e32 v46, v44, v48
	v_max_u32_e32 v47, v34, v51
	v_min_u32_e32 v44, v34, v51
	v_ashrrev_i32_e32 v34, 31, v36
	v_max_u32_e32 v61, v37, v55
	v_min_u32_e32 v58, v37, v55
	v_max_u32_e32 v55, v38, v42
	v_max_u32_e32 v60, v40, v46
	v_bitop3_b32 v34, v36, v34, s13 bitop3:0x93
	v_max_u32_e32 v50, v35, v52
	v_min_u32_e32 v48, v35, v52
	v_max_u32_e32 v67, v55, v60
	v_sub_f32_e32 v35, v34, v34
	v_mul_f32_e32 v35, 0x3fb8aa3b, v35
	v_exp_f32_e32 v64, v35
	v_max_u32_e32 v52, v47, v56
	v_ashrrev_i32_e32 v35, 31, v67
	v_max_u32_e32 v57, v50, v61
	v_bitop3_b32 v35, v67, v35, s13 bitop3:0x93
	v_max_u32_e32 v66, v52, v57
	v_sub_f32_e32 v35, v35, v34
	v_mul_f32_e32 v35, 0x3fb8aa3b, v35
	v_exp_f32_e32 v43, v35
	v_max_u32_e32 v51, v44, v54
	v_ashrrev_i32_e32 v35, 31, v66
	v_max_u32_e32 v53, v48, v58
	v_bitop3_b32 v35, v66, v35, s13 bitop3:0x93
	v_max_u32_e32 v65, v51, v53
	v_sub_f32_e32 v35, v35, v34
	v_mul_f32_e32 v35, 0x3fb8aa3b, v35
	v_cmp_lt_i32_e32 vcc, -1, v65
	v_exp_f32_e32 v37, v35
	v_mov_b32_e32 v63, v64
	v_cndmask_b32_e64 v35, v132, -1, vcc
	v_bitop3_b32 v35, v35, v65, s60 bitop3:0x78
	v_sub_f32_e32 v35, v35, v34
	v_mul_f32_e32 v35, 0x3fb8aa3b, v35
	v_exp_f32_e32 v35, v35
	s_and_saveexec_b64 s[0:1], s[42:43]
	s_cbranch_execz .LBB0_747
	v_cmp_lt_i32_e32 vcc, 1, v1
	v_mov_b32_e32 v63, v43
	s_and_saveexec_b64 s[4:5], vcc
	s_cbranch_execz .LBB0_746
	v_cmp_ne_u32_e32 vcc, 2, v1
	s_and_saveexec_b64 s[6:7], vcc
	s_xor_b64 s[6:7], exec, s[6:7]
	s_or_saveexec_b64 s[6:7], s[6:7]
	v_mov_b32_e32 v63, v35
	s_xor_b64 exec, exec, s[6:7]
	v_mov_b32_e32 v65, v66
	v_mov_b32_e32 v63, v37
	s_or_b64 exec, exec, s[6:7]
	v_mov_b32_e32 v67, v65

; __device__ __forceinline__ float unmono(unsigned u) { return __uint_as_float((u & 0x80000000u) ? (u ^ 0x80000000u) : ~u); }
; __device__ __forceinline__ void topk_phase(LAS unsigned char* lds, const bf16_t* qp, const bf16_t* keys, const float* SU, const float* SV, int* sel_e, float* sel_g, float* sel_su, int G, int b) {
;     ...
;         {
;             const float vmax = unmono(ck[0] & ~255u);
;             float esum = 0.f;
; #pragma unroll
;             for (int k = 0; k < 16; ++k) esum += __expf(unmono(ck[k] & ~255u) - vmax);
;             const float einv = 1.0f / esum;
; #pragma unroll
;             for (int kk = 0; kk < 4; ++kk) {
;                 const unsigned W = fq == 0 ? ck[kk] : fq == 1 ? ck[4 + kk] : fq == 2 ? ck[8 + kk] : ck[12 + kk];
;                 const int k = fq * 4 + kk;
;                 const unsigned id = 255u - (W & 255u);
;                 const unsigned e1 = 127u - (wl[id >> 4] & 127u), e2 = 127u - (wl[16 + (id & 15u)] & 127u);
;                 const size_t o = ((size_t)tok * 8 + h) * 16 + k;
;                 const unsigned ex = e1 * 128u + e2;
;                 sel_e[o] = (int)ex; sel_g[o] = __expf(unmono(W & ~255u) - vmax) * einv * SV[ex]; sel_su[o] = SU[ex];
.LBB0_747:
	s_or_b64 exec, exec, s[0:1]
	v_min_u32_e32 v44, v44, v54
	v_min_u32_e32 v54, v48, v58
	v_min_u32_e32 v58, v59, v62
	v_min_u32_e32 v39, v39, v45
	v_min_u32_e32 v41, v41, v49
	v_min_u32_e32 v38, v38, v42
	v_min_u32_e32 v42, v40, v46
	v_min_u32_e32 v46, v50, v61
	v_max_u32_e32 v49, v39, v41
	v_min_u32_e32 v40, v39, v41
	v_max_u32_e32 v50, v44, v54
	v_min_u32_e32 v41, v44, v54
	v_ashrrev_i32_e32 v44, 31, v58
	v_bitop3_b32 v44, v58, v44, s13 bitop3:0x93
	v_sub_f32_e32 v44, v44, v34
	v_mul_f32_e32 v44, 0x3fb8aa3b, v44
	v_min_u32_e32 v45, v47, v56
	v_min_u32_e32 v56, v55, v60
	v_min_u32_e32 v55, v52, v57
	v_exp_f32_e32 v57, v44
	v_ashrrev_i32_e32 v44, 31, v49
	v_bitop3_b32 v44, v49, v44, s13 bitop3:0x93
	v_sub_f32_e32 v44, v44, v34
	v_mul_f32_e32 v44, 0x3fb8aa3b, v44
	v_min_u32_e32 v59, v51, v53
	v_exp_f32_e32 v51, v44
	v_max_u32_e32 v48, v38, v42
	v_min_u32_e32 v39, v38, v42
	v_add_f32_e32 v42, 0, v64
	v_add_f32_e32 v42, v57, v42
	v_add_f32_e32 v44, v51, v42
	v_max_u32_e32 v47, v45, v46
	v_ashrrev_i32_e32 v42, 31, v40
	v_bitop3_b32 v42, v40, v42, s13 bitop3:0x93
	v_sub_f32_e32 v42, v42, v34
	v_mul_f32_e32 v42, 0x3fb8aa3b, v42
	v_exp_f32_e32 v42, v42
	v_min_u32_e32 v38, v45, v46
	s_ashr_i32 s57, s56, 31
	v_add_f32_e32 v44, v42, v44
	v_add_f32_e32 v43, v43, v44
	v_ashrrev_i32_e32 v44, 31, v56
	v_bitop3_b32 v44, v56, v44, s13 bitop3:0x93
	v_sub_f32_e32 v44, v44, v34
	v_mul_f32_e32 v44, 0x3fb8aa3b, v44
	v_exp_f32_e32 v60, v44
	s_nop 0
	v_ashrrev_i32_e32 v44, 31, v48
	v_bitop3_b32 v44, v48, v44, s13 bitop3:0x93
	v_sub_f32_e32 v44, v44, v34
	v_mul_f32_e32 v44, 0x3fb8aa3b, v44
	v_exp_f32_e32 v52, v44
	v_add_f32_e32 v43, v60, v43
	v_ashrrev_i32_e32 v44, 31, v39
	v_bitop3_b32 v44, v39, v44, s13 bitop3:0x93
	v_sub_f32_e32 v44, v44, v34
	v_mul_f32_e32 v44, 0x3fb8aa3b, v44
	v_exp_f32_e32 v44, v44
	v_add_f32_e32 v43, v52, v43
	v_add_f32_e32 v43, v44, v43
	v_add_f32_e32 v37, v37, v43
	v_ashrrev_i32_e32 v43, 31, v55
	v_bitop3_b32 v43, v55, v43, s13 bitop3:0x93
	v_sub_f32_e32 v43, v43, v34
	v_mul_f32_e32 v43, 0x3fb8aa3b, v43
	v_exp_f32_e32 v61, v43
	s_nop 0
	v_ashrrev_i32_e32 v43, 31, v47
	v_bitop3_b32 v43, v47, v43, s13 bitop3:0x93
	v_sub_f32_e32 v43, v43, v34
	v_mul_f32_e32 v43, 0x3fb8aa3b, v43
	v_exp_f32_e32 v53, v43
	v_add_f32_e32 v37, v61, v37
	v_ashrrev_i32_e32 v43, 31, v38
	v_bitop3_b32 v43, v38, v43, s13 bitop3:0x93
	v_sub_f32_e32 v43, v43, v34
	v_mul_f32_e32 v43, 0x3fb8aa3b, v43
	v_exp_f32_e32 v45, v43
	v_add_f32_e32 v37, v53, v37
	v_add_f32_e32 v37, v45, v37
	v_add_f32_e32 v35, v35, v37
	v_ashrrev_i32_e32 v37, 31, v59
	v_bitop3_b32 v37, v59, v37, s13 bitop3:0x93
	v_sub_f32_e32 v37, v37, v34
	v_mul_f32_e32 v37, 0x3fb8aa3b, v37
	v_exp_f32_e32 v62, v37
	s_nop 0
	v_ashrrev_i32_e32 v37, 31, v50
	v_bitop3_b32 v37, v50, v37, s13 bitop3:0x93
	v_sub_f32_e32 v37, v37, v34
	v_mul_f32_e32 v37, 0x3fb8aa3b, v37
	v_cmp_lt_i32_e32 vcc, -1, v41
	v_exp_f32_e32 v54, v37
	v_add_f32_e32 v35, v62, v35
	v_cndmask_b32_e64 v37, v132, -1, vcc
	v_bitop3_b32 v37, v37, v41, s60 bitop3:0x78
	v_sub_f32_e32 v34, v37, v34
	v_mul_f32_e32 v34, 0x3fb8aa3b, v34
	v_exp_f32_e32 v46, v34
	v_add_f32_e32 v35, v54, v35
	v_add_f32_e32 v34, v46, v35
	v_div_scale_f32 v35, s[0:1], v34, v34, 1.0
	v_rcp_f32_e32 v37, v35
	s_nop 0
	v_fma_f32 v43, -v35, v37, 1.0
	v_fmac_f32_e32 v37, v43, v37
	v_div_scale_f32 v43, vcc, 1.0, v34, 1.0
	v_mul_f32_e32 v64, v43, v37
	v_fma_f32 v65, -v35, v64, v43
	v_fmac_f32_e32 v64, v65, v37
	v_fma_f32 v35, -v35, v64, v43
	v_div_fmas_f32 v35, v35, v37, v64
	v_not_b32_e32 v37, v36
	v_lshrrev_b32_e32 v37, 2, v37
	v_and_b32_e32 v37, 60, v37
	v_bitop3_b32 v36, v36, 15, v36 bitop3:0xc
	v_add_u32_e32 v37, v83, v37
	v_lshl_add_u32 v36, v36, 2, v83
	ds_read_b32 v64, v37
	ds_read_b32 v36, v36 offset:64
	v_div_fixup_f32 v43, v35, v34, 1.0
	v_lshlrev_b64 v[34:35], 7, v[94:95]
	v_lshl_add_u64 v[34:35], s[56:57], 4, v[34:35]
	v_mov_b32_e32 v37, v35
	s_waitcnt lgkmcnt(0)
	v_and_b32_e32 v65, 0x7f, v36
	v_or_b32_e32 v36, v34, v82
	v_lshlrev_b32_e32 v64, 7, v64
	v_and_b32_e32 v64, 0x3f80, v64
	v_lshlrev_b64 v[36:37], 2, v[36:37]
	v_bitop3_b32 v66, v65, s61, v64 bitop3:0x36
	v_lshl_add_u64 v[64:65], s[46:47], 0, v[36:37]
	global_store_dword v[64:65], v66, off
	v_lshlrev_b32_e32 v66, 2, v66
	global_load_dword v170, v66, s[50:51]
	global_load_dword v171, v66, s[86:87]
	v_mul_f32_e32 v172, v43, v63
	v_mov_b64_e32 v[174:175], v[36:37]
	s_and_saveexec_b64 s[0:1], s[42:43]
	s_cbranch_execz .LBB0_755
	v_cmp_lt_i32_e32 vcc, 1, v1
	s_and_saveexec_b64 s[4:5], vcc
	s_xor_b64 s[4:5], exec, s[4:5]
	s_cbranch_execz .LBB0_752
	v_cmp_ne_u32_e32 vcc, 2, v1
	s_and_saveexec_b64 s[6:7], vcc
	v_mov_b32_e32 v55, v59
	v_mov_b32_e32 v61, v62
	s_or_b64 exec, exec, s[6:7]
